# P2: next unit's A-stage DMAs issued before the epilogue stores; first K iteration's waits do not cover the stores
# baseline (speedup 1.0000x reference)
.LBB0_194:
	s_add_i32 s55, s27, 0x18000
	s_mov_b64 s[20:21], 0x80
	s_bfe_u32 s6, s61, 0x20006
	v_lshl_add_u64 v[6:7], v[6:7], 0, s[20:21]
	s_mov_b32 m0, s55
	s_add_i32 s56, s27, 0x1a000
	s_lshl_b32 s7, s16, 13
	s_lshl_b32 s54, s6, 5
	s_lshl_b32 s22, s6, 12
	s_waitcnt vmcnt(2)
	s_barrier
	global_load_lds_dwordx4 v[6:7], off
	v_lshl_add_u64 v[4:5], v[4:5], 0, s[20:21]
	s_mov_b32 m0, s56
	s_add_i32 s57, s27, 0x8000
	s_add_i32 s58, s27, 0xa000
	global_load_lds_dwordx4 v[4:5], off
	v_lshl_add_u64 v[0:1], v[0:1], 0, s[20:21]
	s_mov_b32 m0, s57
	s_add_u32 s4, s44, 0x80080
	global_load_lds_dwordx4 v[0:1], off
	v_lshl_add_u64 v[0:1], v[2:3], 0, s[20:21]
	s_mov_b32 m0, s58
	s_addc_u32 s5, s45, 0
	s_add_i32 s59, s27, 0x1c000
	global_load_lds_dwordx4 v[0:1], off
	v_lshl_add_u64 v[0:1], s[4:5], 0, v[162:163]
	s_mov_b32 m0, s59
	s_add_i32 s60, s27, 0x1e000
	global_load_lds_dwordx4 v[0:1], off
	v_lshl_add_u64 v[0:1], s[4:5], 0, v[166:167]
	s_mov_b32 m0, s60
	v_and_b32_e32 v15, 15, v14
	global_load_lds_dwordx4 v[0:1], off
	s_waitcnt vmcnt(0)
	v_bfe_u32 v16, v14, 4, 2
	v_lshlrev_b32_e32 v14, 2, v14
	v_lshlrev_b32_e32 v17, 4, v16
	v_lshlrev_b32_e32 v18, 6, v15
	v_and_b32_e32 v14, 32, v14
	s_add_i32 s22, s22, 0
	v_bitop3_b32 v0, v18, v14, v17 bitop3:0x36
	s_cmpk_lt_u32 s61, 0x100
	v_lshl_or_b32 v171, s16, 6, v15
	v_add_u32_e32 v1, s22, v0
	s_cselect_b64 s[22:23], -1, 0
	s_lshl_b32 s16, s16, 11
	s_add_i32 s16, s16, 0
	v_lshlrev_b32_e32 v2, 5, v15
	s_add_i32 s26, s16, 0x20000
	v_add_u32_e32 v202, s26, v2
	s_add_i32 s26, s16, 0x20200
	v_add_u32_e32 v204, s26, v2
	s_add_i32 s26, s16, 0x20400
	v_add_u32_e32 v206, s26, v2
	s_add_i32 s26, s16, 0x20600
	v_add_u32_e32 v208, s26, v2
	s_add_i32 s26, s16, 0x21000
	v_add_u32_e32 v186, 0x10000, v1
	v_add_u32_e32 v187, 0x10400, v1
	v_add_u32_e32 v188, 0x10800, v1
	v_add_u32_e32 v189, 0x10c00, v1
	v_add_u32_e32 v190, 0x14000, v1
	v_add_u32_e32 v191, 0x14400, v1
	v_add_u32_e32 v192, 0x14800, v1
	v_add_u32_e32 v193, 0x14c00, v1
	v_add_u32_e32 v194, 0x18000, v1
	v_add_u32_e32 v195, 0x18400, v1
	v_add_u32_e32 v196, 0x18800, v1
	v_add_u32_e32 v197, 0x18c00, v1
	v_add_u32_e32 v198, 0x1c000, v1
	v_add_u32_e32 v199, 0x1c400, v1
	v_add_u32_e32 v200, 0x1c800, v1
	v_add_u32_e32 v201, 0x1cc00, v1
	v_add_u32_e32 v210, s26, v2
	s_add_i32 s26, s16, 0x21200
	v_lshlrev_b32_e32 v1, 15, v8
	v_add_u32_e32 v212, s26, v2
	s_add_i32 s26, s16, 0x21400
	s_add_i32 s16, s16, 0x21600
	v_and_b32_e32 v1, 0xffff0000, v1
	v_add_u32_e32 v214, s26, v2
	v_add_u32_e32 v216, s16, v2
	v_lshl_add_u32 v1, v9, 12, v1
	v_and_b32_e32 v2, 1, v8
	v_lshl_or_b32 v1, v2, 6, v1
	v_lshl_add_u32 v172, v10, 1, v1
	v_lshlrev_b32_e32 v1, 15, v11
	v_and_b32_e32 v1, 0xffff0000, v1
	s_waitcnt vmcnt(6)
	v_add_u32_e32 v0, 0, v0
	v_lshl_add_u32 v1, v12, 12, v1
	v_and_b32_e32 v2, 1, v11
	v_lshlrev_b32_e32 v170, 3, v16
	s_lshl_b32 s6, s6, 2
	v_lshl_or_b32 v1, v2, 6, v1
	v_add_u32_e32 v218, s7, v0
	v_mbcnt_lo_u32_b32 v0, -1, 0
	v_cmp_eq_u32_e64 s[4:5], 0, v16
	s_ashr_i32 s61, s46, 31
	s_ashr_i32 s63, s68, 31
	v_add_u32_e32 v203, s6, v202
	v_add_u32_e32 v205, s6, v204
	v_add_u32_e32 v207, s6, v206
	v_add_u32_e32 v209, s6, v208
	v_add_u32_e32 v211, s6, v210
	v_add_u32_e32 v213, s6, v212
	v_add_u32_e32 v215, s6, v214
	v_add_u32_e32 v217, s6, v216
	v_mov_b32_e32 v173, v169
	v_lshl_add_u32 v174, v13, 1, v1
	v_mov_b32_e32 v175, v169
	s_movk_i32 s64, 0x181
	s_mov_b32 s26, 0x3c800000
	v_mov_b32_e32 v219, 0x358637bd
	s_lshl_b32 s16, s54, 1
	v_lshlrev_b32_e32 v168, 1, v170
	v_mbcnt_hi_u32_b32 v220, -1, v0
	s_mov_b32 s65, s17
	s_barrier
	s_mov_b32 s80, 0
	s_branch .LBB0_197

.LBB0_200:
	s_cmp_eq_u32 s80, 1
	s_cselect_b64 vcc, -1, 0
	s_mov_b32 s80, 0
	s_add_u32 s72, s42, 0xfff80000
	s_addc_u32 s73, s43, -1
	s_mov_b32 m0, s57
	s_nop 0
	global_load_lds_dwordx4 v160, s[72:73]
	s_mov_b32 m0, s58
	s_nop 0
	global_load_lds_dwordx4 v164, s[72:73]
	ds_read_b128 v[16:19], v186
	ds_read_b128 v[20:23], v187
	ds_read_b128 v[24:27], v188
	ds_read_b128 v[28:31], v189
	ds_read_b128 v[0:3], v190
	ds_read_b128 v[4:7], v191
	ds_read_b128 v[8:11], v192
	ds_read_b128 v[12:15], v193
	s_add_u32 s44, s42, 0xfff80080
	s_addc_u32 s45, s43, -1
	s_cmp_eq_u32 s68, 28
	s_cselect_b32 s47, s31, s45
	s_cselect_b32 s46, s35, s44
	s_cselect_b32 s45, s29, s67
	s_cselect_b32 s44, s39, s66
	s_add_i32 m0, s27, 0xc000
	ds_read_b128 v[178:181], v218
	ds_read_b128 v[182:185], v218 offset:1024
	ds_read_b128 v[222:225], v218 offset:2048
	ds_read_b128 v[226:229], v218 offset:3072
	ds_read_b128 v[230:233], v218 offset:4096
	ds_read_b128 v[234:237], v218 offset:5120
	ds_read_b128 v[238:241], v218 offset:6144
	ds_read_b128 v[242:245], v218 offset:7168
	global_load_lds_dwordx4 v172, s[42:43]
	s_add_i32 m0, s27, 0xe000
	s_nop 0
	global_load_lds_dwordx4 v174, s[42:43]
	s_cbranch_vccz .Lp2w0n
	s_waitcnt vmcnt(28)
	s_branch .Lp2w0j
.Lp2w0n:
	s_waitcnt vmcnt(8)
.Lp2w0j:
	s_waitcnt lgkmcnt(0)
	s_barrier
	s_setprio 1
	s_waitcnt lgkmcnt(0)
	v_mfma_f32_16x16x128_f8f6f4 v[156:159], v[16:23], v[178:185], v[156:159]
	v_mfma_f32_16x16x128_f8f6f4 v[152:155], v[24:31], v[178:185], v[152:155]
	v_mfma_f32_16x16x128_f8f6f4 v[148:151], v[16:23], v[222:229], v[148:151]
	v_mfma_f32_16x16x128_f8f6f4 v[144:147], v[24:31], v[222:229], v[144:147]
	v_mfma_f32_16x16x128_f8f6f4 v[140:143], v[16:23], v[230:237], v[140:143]
	v_mfma_f32_16x16x128_f8f6f4 v[136:139], v[24:31], v[230:237], v[136:139]
	v_mfma_f32_16x16x128_f8f6f4 v[132:135], v[16:23], v[238:245], v[132:135]
	v_mfma_f32_16x16x128_f8f6f4 v[128:131], v[24:31], v[238:245], v[128:131]
	s_setprio 0
	s_setprio 1
	v_mfma_f32_16x16x128_f8f6f4 v[124:127], v[0:7], v[178:185], v[124:127]
	v_mfma_f32_16x16x128_f8f6f4 v[120:123], v[8:15], v[178:185], v[120:123]
	v_mfma_f32_16x16x128_f8f6f4 v[116:119], v[0:7], v[222:229], v[116:119]
	v_mfma_f32_16x16x128_f8f6f4 v[112:115], v[8:15], v[222:229], v[112:115]
	v_mfma_f32_16x16x128_f8f6f4 v[108:111], v[0:7], v[230:237], v[108:111]
	v_mfma_f32_16x16x128_f8f6f4 v[104:107], v[8:15], v[230:237], v[104:107]
	v_mfma_f32_16x16x128_f8f6f4 v[100:103], v[0:7], v[238:245], v[100:103]
	v_mfma_f32_16x16x128_f8f6f4 v[96:99], v[8:15], v[238:245], v[96:99]
	s_setprio 0
	s_barrier
	s_mov_b32 m0, s33
	v_lshl_add_u64 v[178:179], s[44:45], 0, v[162:163]
	s_add_u32 s70, s44, 0x80000
	ds_read_b128 v[222:225], v218 offset:16384
	ds_read_b128 v[226:229], v218 offset:17408
	ds_read_b128 v[230:233], v218 offset:18432
	ds_read_b128 v[234:237], v218 offset:19456
	ds_read_b128 v[238:241], v218 offset:20480
	ds_read_b128 v[242:245], v218 offset:21504
	ds_read_b128 v[246:249], v218 offset:22528
	ds_read_b128 v[250:253], v218 offset:23552
	global_load_lds_dwordx4 v[178:179], off
	v_lshl_add_u64 v[180:181], s[44:45], 0, v[166:167]
	s_mov_b32 m0, s48
	s_addc_u32 s71, s45, 0
	global_load_lds_dwordx4 v[180:181], off
	s_mov_b32 m0, s49
	s_nop 0
	global_load_lds_dwordx4 v162, s[70:71]
	s_mov_b32 m0, s50
	s_nop 0
	global_load_lds_dwordx4 v166, s[70:71]
	s_cbranch_vccz .Lp2w1n
	s_waitcnt vmcnt(26)
	s_branch .Lp2w1j
.Lp2w1n:
	s_waitcnt vmcnt(6)
.Lp2w1j:
	s_waitcnt lgkmcnt(0)
	s_barrier
	s_setprio 1
	s_waitcnt lgkmcnt(0)
	v_mfma_f32_16x16x128_f8f6f4 v[92:95], v[16:23], v[222:229], v[92:95]
	v_mfma_f32_16x16x128_f8f6f4 v[88:91], v[24:31], v[222:229], v[88:91]
	v_mfma_f32_16x16x128_f8f6f4 v[84:87], v[16:23], v[230:237], v[84:87]
	v_mfma_f32_16x16x128_f8f6f4 v[80:83], v[24:31], v[230:237], v[80:83]
	v_mfma_f32_16x16x128_f8f6f4 v[76:79], v[16:23], v[238:245], v[76:79]
	v_mfma_f32_16x16x128_f8f6f4 v[72:75], v[24:31], v[238:245], v[72:75]
	v_mfma_f32_16x16x128_f8f6f4 v[68:71], v[16:23], v[246:253], v[68:71]
	v_mfma_f32_16x16x128_f8f6f4 v[64:67], v[24:31], v[246:253], v[64:67]
	s_setprio 0
	s_setprio 1
	v_mfma_f32_16x16x128_f8f6f4 v[60:63], v[0:7], v[222:229], v[60:63]
	v_mfma_f32_16x16x128_f8f6f4 v[56:59], v[8:15], v[222:229], v[56:59]
	v_mfma_f32_16x16x128_f8f6f4 v[52:55], v[0:7], v[230:237], v[52:55]
	v_mfma_f32_16x16x128_f8f6f4 v[48:51], v[8:15], v[230:237], v[48:51]
	v_mfma_f32_16x16x128_f8f6f4 v[44:47], v[0:7], v[238:245], v[44:47]
	v_mfma_f32_16x16x128_f8f6f4 v[40:43], v[8:15], v[238:245], v[40:43]
	v_mfma_f32_16x16x128_f8f6f4 v[36:39], v[0:7], v[246:253], v[36:39]
	v_mfma_f32_16x16x128_f8f6f4 v[32:35], v[8:15], v[246:253], v[32:35]
	s_setprio 0
	s_barrier
	s_mov_b32 m0, s27
	s_nop 0
	global_load_lds_dwordx4 v160, s[46:47]
	s_mov_b32 m0, s51
	s_nop 0
	global_load_lds_dwordx4 v164, s[46:47]
	ds_read_b128 v[0:3], v194
	ds_read_b128 v[4:7], v195
	ds_read_b128 v[8:11], v196
	ds_read_b128 v[12:15], v197
	ds_read_b128 v[16:19], v198
	ds_read_b128 v[20:23], v199
	ds_read_b128 v[24:27], v200
	ds_read_b128 v[28:31], v201
	s_add_u32 s46, s46, 0x80000
	s_addc_u32 s47, s47, 0
	s_mov_b32 m0, s52
	ds_read_b128 v[222:225], v218 offset:32768
	ds_read_b128 v[226:229], v218 offset:33792
	ds_read_b128 v[230:233], v218 offset:34816
	ds_read_b128 v[234:237], v218 offset:35840
	ds_read_b128 v[238:241], v218 offset:36864
	ds_read_b128 v[242:245], v218 offset:37888
	ds_read_b128 v[246:249], v218 offset:38912
	ds_read_b128 v[250:253], v218 offset:39936
	global_load_lds_dwordx4 v160, s[46:47]
	s_mov_b32 m0, s53
	s_nop 0
	global_load_lds_dwordx4 v164, s[46:47]
	s_cbranch_vccz .Lp2w2n
	s_waitcnt vmcnt(28)
	s_branch .Lp2w2j

.Lp2w2j:
	s_waitcnt lgkmcnt(0)
	s_barrier
	s_setprio 1
	s_waitcnt lgkmcnt(0)
	v_mfma_f32_16x16x128_f8f6f4 v[156:159], v[0:7], v[222:229], v[156:159]
	v_mfma_f32_16x16x128_f8f6f4 v[152:155], v[8:15], v[222:229], v[152:155]
	v_mfma_f32_16x16x128_f8f6f4 v[148:151], v[0:7], v[230:237], v[148:151]
	v_mfma_f32_16x16x128_f8f6f4 v[144:147], v[8:15], v[230:237], v[144:147]
	v_mfma_f32_16x16x128_f8f6f4 v[140:143], v[0:7], v[238:245], v[140:143]
	v_mfma_f32_16x16x128_f8f6f4 v[136:139], v[8:15], v[238:245], v[136:139]
	v_mfma_f32_16x16x128_f8f6f4 v[132:135], v[0:7], v[246:253], v[132:135]
	v_mfma_f32_16x16x128_f8f6f4 v[128:131], v[8:15], v[246:253], v[128:131]
	s_setprio 0
	s_setprio 1
	v_mfma_f32_16x16x128_f8f6f4 v[124:127], v[16:23], v[222:229], v[124:127]
	v_mfma_f32_16x16x128_f8f6f4 v[120:123], v[24:31], v[222:229], v[120:123]
	v_mfma_f32_16x16x128_f8f6f4 v[116:119], v[16:23], v[230:237], v[116:119]
	v_mfma_f32_16x16x128_f8f6f4 v[112:115], v[24:31], v[230:237], v[112:115]
	v_mfma_f32_16x16x128_f8f6f4 v[108:111], v[16:23], v[238:245], v[108:111]
	v_mfma_f32_16x16x128_f8f6f4 v[104:107], v[24:31], v[238:245], v[104:107]
	v_mfma_f32_16x16x128_f8f6f4 v[100:103], v[16:23], v[246:253], v[100:103]
	v_mfma_f32_16x16x128_f8f6f4 v[96:99], v[24:31], v[246:253], v[96:99]
	s_setprio 0
	s_barrier
	s_mov_b32 m0, s55
	v_lshl_add_u64 v[176:177], v[178:179], 0, s[20:21]
	s_add_u32 s44, s44, 0x80080
	ds_read_b128 v[222:225], v218 offset:49152
	ds_read_b128 v[226:229], v218 offset:50176
	ds_read_b128 v[230:233], v218 offset:51200
	ds_read_b128 v[234:237], v218 offset:52224
	ds_read_b128 v[238:241], v218 offset:53248
	ds_read_b128 v[242:245], v218 offset:54272
	ds_read_b128 v[246:249], v218 offset:55296
	ds_read_b128 v[250:253], v218 offset:56320
	global_load_lds_dwordx4 v[176:177], off
	v_lshl_add_u64 v[176:177], v[180:181], 0, s[20:21]
	s_mov_b32 m0, s56
	s_addc_u32 s45, s45, 0
	global_load_lds_dwordx4 v[176:177], off
	s_mov_b32 m0, s59
	s_nop 0
	global_load_lds_dwordx4 v162, s[44:45]
	s_mov_b32 m0, s60
	s_nop 0
	global_load_lds_dwordx4 v166, s[44:45]
	s_waitcnt vmcnt(6)
	s_waitcnt lgkmcnt(0)
	s_barrier
	s_setprio 1
	s_waitcnt lgkmcnt(0)
	v_mfma_f32_16x16x128_f8f6f4 v[92:95], v[0:7], v[222:229], v[92:95]
	v_mfma_f32_16x16x128_f8f6f4 v[88:91], v[8:15], v[222:229], v[88:91]
	v_mfma_f32_16x16x128_f8f6f4 v[84:87], v[0:7], v[230:237], v[84:87]
	v_mfma_f32_16x16x128_f8f6f4 v[80:83], v[8:15], v[230:237], v[80:83]
	v_mfma_f32_16x16x128_f8f6f4 v[76:79], v[0:7], v[238:245], v[76:79]
	v_mfma_f32_16x16x128_f8f6f4 v[72:75], v[8:15], v[238:245], v[72:75]
	v_mfma_f32_16x16x128_f8f6f4 v[68:71], v[0:7], v[246:253], v[68:71]
	v_mfma_f32_16x16x128_f8f6f4 v[64:67], v[8:15], v[246:253], v[64:67]
	s_setprio 0
	s_setprio 1
	v_mfma_f32_16x16x128_f8f6f4 v[60:63], v[16:23], v[222:229], v[60:63]
	v_mfma_f32_16x16x128_f8f6f4 v[56:59], v[24:31], v[222:229], v[56:59]
	v_mfma_f32_16x16x128_f8f6f4 v[52:55], v[16:23], v[230:237], v[52:55]
	v_mfma_f32_16x16x128_f8f6f4 v[48:51], v[24:31], v[230:237], v[48:51]
	v_mfma_f32_16x16x128_f8f6f4 v[44:47], v[16:23], v[238:245], v[44:47]
	v_mfma_f32_16x16x128_f8f6f4 v[40:43], v[24:31], v[238:245], v[40:43]
	v_mfma_f32_16x16x128_f8f6f4 v[36:39], v[16:23], v[246:253], v[36:39]
	v_mfma_f32_16x16x128_f8f6f4 v[32:35], v[24:31], v[246:253], v[32:35]
	s_setprio 0
	s_barrier
	s_add_i32 s68, s68, 2
	s_add_u32 s42, s42, 0x100
	s_addc_u32 s43, s43, 0
	s_add_u32 s66, s66, 0x100
	s_addc_u32 s67, s67, 0
	s_cmp_gt_u32 s68, 29
	s_cbranch_scc0 .LBB0_200
	s_nop 15
	s_nop 15
	s_and_b64 vcc, exec, s[22:23]
	s_cbranch_vccz .LBB0_203
	s_barrier

.LBB0_246:
	s_add_u32 s76, s36, 0xfff80000
	s_addc_u32 s77, s37, -1
	s_mov_b32 m0, s57
	s_nop 0
	global_load_lds_dwordx4 v160, s[76:77]
	s_mov_b32 m0, s58
	s_nop 0
	global_load_lds_dwordx4 v164, s[76:77]
	s_add_i32 m0, s27, 0xc000
	s_nop 0
	global_load_lds_dwordx4 v172, s[36:37]
	s_add_i32 m0, s27, 0xe000
	s_nop 0
	global_load_lds_dwordx4 v174, s[36:37]
	s_mov_b32 s80, 1
	s_lshl_b32 s29, s38, 8
	s_lshl_b32 s38, s34, 1
	s_ashr_i32 s39, s38, 31
	s_lshl_b64 s[34:35], s[38:39], 22
	v_readlane_b32 s44, v254, 14
	v_readlane_b32 s45, v254, 15
	s_add_u32 s34, s44, s34
	s_addc_u32 s35, s45, s35
	s_or_b32 s38, s38, 1
	v_add_u32_e32 v0, s29, v171
	s_ashr_i32 s39, s38, 31
	v_ashrrev_i32_e32 v1, 31, v0
	s_lshl_b64 s[38:39], s[38:39], 22
	v_lshlrev_b64 v[4:5], 8, v[0:1]
	s_add_u32 s38, s44, s38
	v_lshl_add_u64 v[6:7], s[34:35], 0, v[4:5]
	s_addc_u32 s39, s45, s39
	v_lshl_add_u64 v[6:7], v[6:7], 0, s[16:17]
	v_lshl_add_u64 v[4:5], s[38:39], 0, v[4:5]
	v_cvt_pk_bf16_f32 v0, v156, v157
	v_lshl_add_u64 v[6:7], v[6:7], 0, v[168:169]
	v_lshl_add_u64 v[4:5], v[4:5], 0, s[16:17]
	v_cvt_pk_bf16_f32 v1, v158, v159
	v_cvt_pk_bf16_f32 v2, v152, v153
	v_cvt_pk_bf16_f32 v3, v154, v155
	global_store_dwordx4 v[6:7], v[0:3], off
	v_lshl_add_u64 v[4:5], v[4:5], 0, v[168:169]
	s_andn2_b64 vcc, exec, s[42:43]
	v_cvt_pk_bf16_f32 v0, v178, v179
	v_cvt_pk_bf16_f32 v1, v126, v127
	v_cvt_pk_bf16_f32 v2, v180, v181
	v_cvt_pk_bf16_f32 v3, v124, v125
	global_store_dwordx4 v[4:5], v[0:3], off
	s_nop 1
	v_or_b32_e32 v0, 16, v171
	v_add_u32_e32 v0, s29, v0
	v_ashrrev_i32_e32 v1, 31, v0
	v_lshlrev_b64 v[4:5], 8, v[0:1]
	v_lshl_add_u64 v[6:7], s[34:35], 0, v[4:5]
	v_lshl_add_u64 v[6:7], v[6:7], 0, s[16:17]
	v_lshl_add_u64 v[4:5], s[38:39], 0, v[4:5]
	v_cvt_pk_bf16_f32 v0, v148, v149
	v_lshl_add_u64 v[6:7], v[6:7], 0, v[168:169]
	v_lshl_add_u64 v[4:5], v[4:5], 0, s[16:17]
	v_cvt_pk_bf16_f32 v1, v150, v151
	v_cvt_pk_bf16_f32 v2, v144, v145
	v_cvt_pk_bf16_f32 v3, v146, v147
	global_store_dwordx4 v[6:7], v[0:3], off
	v_lshl_add_u64 v[4:5], v[4:5], 0, v[168:169]
	s_nop 0
	v_cvt_pk_bf16_f32 v0, v120, v121
	v_cvt_pk_bf16_f32 v1, v118, v119
	v_cvt_pk_bf16_f32 v2, v122, v123
	v_cvt_pk_bf16_f32 v3, v116, v117
	global_store_dwordx4 v[4:5], v[0:3], off
	s_nop 1
	v_or_b32_e32 v0, 32, v171
	v_add_u32_e32 v0, s29, v0
	v_ashrrev_i32_e32 v1, 31, v0
	v_lshlrev_b64 v[4:5], 8, v[0:1]
	v_lshl_add_u64 v[6:7], s[34:35], 0, v[4:5]
	v_lshl_add_u64 v[6:7], v[6:7], 0, s[16:17]
	v_lshl_add_u64 v[4:5], s[38:39], 0, v[4:5]
	v_cvt_pk_bf16_f32 v0, v140, v141
	v_lshl_add_u64 v[6:7], v[6:7], 0, v[168:169]
	v_lshl_add_u64 v[4:5], v[4:5], 0, s[16:17]
	v_cvt_pk_bf16_f32 v1, v142, v143
	v_cvt_pk_bf16_f32 v2, v136, v137
	v_cvt_pk_bf16_f32 v3, v138, v139
	global_store_dwordx4 v[6:7], v[0:3], off
	v_lshl_add_u64 v[4:5], v[4:5], 0, v[168:169]
	s_nop 0
	v_cvt_pk_bf16_f32 v0, v108, v109
	v_cvt_pk_bf16_f32 v1, v110, v111
	v_cvt_pk_bf16_f32 v2, v112, v113
	v_cvt_pk_bf16_f32 v3, v106, v107
	global_store_dwordx4 v[4:5], v[0:3], off
	s_nop 1
	v_or_b32_e32 v0, 48, v171
	v_add_u32_e32 v0, s29, v0
	v_ashrrev_i32_e32 v1, 31, v0
	v_lshlrev_b64 v[4:5], 8, v[0:1]
	v_lshl_add_u64 v[6:7], s[34:35], 0, v[4:5]
	v_lshl_add_u64 v[6:7], v[6:7], 0, s[16:17]
	v_lshl_add_u64 v[4:5], s[38:39], 0, v[4:5]
	v_cvt_pk_bf16_f32 v0, v132, v133
	v_lshl_add_u64 v[6:7], v[6:7], 0, v[168:169]
	v_lshl_add_u64 v[4:5], v[4:5], 0, s[16:17]
	v_cvt_pk_bf16_f32 v1, v134, v135
	v_cvt_pk_bf16_f32 v2, v128, v129
	v_cvt_pk_bf16_f32 v3, v130, v131
	global_store_dwordx4 v[6:7], v[0:3], off
	v_lshl_add_u64 v[4:5], v[4:5], 0, v[168:169]
	s_nop 0
	v_cvt_pk_bf16_f32 v0, v100, v101
	v_cvt_pk_bf16_f32 v1, v102, v103
	v_cvt_pk_bf16_f32 v2, v96, v97
	v_cvt_pk_bf16_f32 v3, v98, v99
	global_store_dwordx4 v[4:5], v[0:3], off
	s_nop 1
	v_add_u32_e32 v0, 0x80, v171
	v_add_u32_e32 v0, s29, v0
	v_ashrrev_i32_e32 v1, 31, v0
	v_lshlrev_b64 v[4:5], 8, v[0:1]
	v_lshl_add_u64 v[6:7], s[34:35], 0, v[4:5]
	v_lshl_add_u64 v[6:7], v[6:7], 0, s[16:17]
	v_lshl_add_u64 v[4:5], s[38:39], 0, v[4:5]
	v_cvt_pk_bf16_f32 v0, v92, v93
	v_lshl_add_u64 v[6:7], v[6:7], 0, v[168:169]
	v_lshl_add_u64 v[4:5], v[4:5], 0, s[16:17]
	v_cvt_pk_bf16_f32 v1, v94, v95
	v_cvt_pk_bf16_f32 v2, v88, v89
	v_cvt_pk_bf16_f32 v3, v90, v91
	global_store_dwordx4 v[6:7], v[0:3], off
	v_lshl_add_u64 v[4:5], v[4:5], 0, v[168:169]
	s_nop 0
	v_cvt_pk_bf16_f32 v0, v104, v105
	v_cvt_pk_bf16_f32 v1, v62, v63
	v_cvt_pk_bf16_f32 v2, v114, v115
	v_cvt_pk_bf16_f32 v3, v60, v61
	global_store_dwordx4 v[4:5], v[0:3], off
	s_nop 1
	v_add_u32_e32 v0, 0x90, v171
	v_add_u32_e32 v0, s29, v0
	v_ashrrev_i32_e32 v1, 31, v0
	v_lshlrev_b64 v[4:5], 8, v[0:1]
	v_lshl_add_u64 v[6:7], s[34:35], 0, v[4:5]
	v_lshl_add_u64 v[6:7], v[6:7], 0, s[16:17]
	v_lshl_add_u64 v[4:5], s[38:39], 0, v[4:5]
	v_cvt_pk_bf16_f32 v0, v84, v85
	v_lshl_add_u64 v[6:7], v[6:7], 0, v[168:169]
	v_lshl_add_u64 v[4:5], v[4:5], 0, s[16:17]
	v_cvt_pk_bf16_f32 v1, v86, v87
	v_cvt_pk_bf16_f32 v2, v80, v81
	v_cvt_pk_bf16_f32 v3, v82, v83
	global_store_dwordx4 v[6:7], v[0:3], off
	v_lshl_add_u64 v[4:5], v[4:5], 0, v[168:169]
	s_nop 0
	v_cvt_pk_bf16_f32 v0, v56, v57
	v_cvt_pk_bf16_f32 v1, v54, v55
	v_cvt_pk_bf16_f32 v2, v58, v59
	v_cvt_pk_bf16_f32 v3, v52, v53
	global_store_dwordx4 v[4:5], v[0:3], off
	s_nop 1
	v_add_u32_e32 v0, 0xa0, v171
	v_add_u32_e32 v0, s29, v0
	v_ashrrev_i32_e32 v1, 31, v0
	v_lshlrev_b64 v[4:5], 8, v[0:1]
	v_lshl_add_u64 v[6:7], s[34:35], 0, v[4:5]
	v_lshl_add_u64 v[6:7], v[6:7], 0, s[16:17]
	v_lshl_add_u64 v[4:5], s[38:39], 0, v[4:5]
	v_cvt_pk_bf16_f32 v0, v76, v77
	v_lshl_add_u64 v[6:7], v[6:7], 0, v[168:169]
	v_lshl_add_u64 v[4:5], v[4:5], 0, s[16:17]
	v_cvt_pk_bf16_f32 v1, v78, v79
	v_cvt_pk_bf16_f32 v2, v72, v73
	v_cvt_pk_bf16_f32 v3, v74, v75
	global_store_dwordx4 v[6:7], v[0:3], off
	v_lshl_add_u64 v[4:5], v[4:5], 0, v[168:169]
	s_nop 0
	v_cvt_pk_bf16_f32 v0, v48, v49
	v_cvt_pk_bf16_f32 v1, v46, v47
	v_cvt_pk_bf16_f32 v2, v50, v51
	v_cvt_pk_bf16_f32 v3, v44, v45
	global_store_dwordx4 v[4:5], v[0:3], off
	s_nop 1
	v_add_u32_e32 v0, 0xb0, v171
	v_add_u32_e32 v0, s29, v0
	v_ashrrev_i32_e32 v1, 31, v0
	v_lshlrev_b64 v[4:5], 8, v[0:1]
	v_lshl_add_u64 v[6:7], s[34:35], 0, v[4:5]
	v_lshl_add_u64 v[4:5], s[38:39], 0, v[4:5]
	v_lshl_add_u64 v[6:7], v[6:7], 0, s[16:17]
	v_lshl_add_u64 v[4:5], v[4:5], 0, s[16:17]
	v_cvt_pk_bf16_f32 v0, v68, v69
	v_cvt_pk_bf16_f32 v1, v70, v71
	v_cvt_pk_bf16_f32 v2, v64, v65
	v_cvt_pk_bf16_f32 v3, v66, v67
	v_lshl_add_u64 v[6:7], v[6:7], 0, v[168:169]
	v_lshl_add_u64 v[4:5], v[4:5], 0, v[168:169]
	global_store_dwordx4 v[6:7], v[0:3], off
	s_nop 1
	v_cvt_pk_bf16_f32 v0, v40, v41
	v_cvt_pk_bf16_f32 v1, v38, v39
	v_cvt_pk_bf16_f32 v2, v42, v43
	v_cvt_pk_bf16_f32 v3, v36, v37
	global_store_dwordx4 v[4:5], v[0:3], off
	s_cbranch_vccnz .LBB0_248
	s_waitcnt lgkmcnt(0)
	s_barrier
